# v3 + P4 group-norm gains staged once in spare LDS and read by ds_read_b128 in every chunk final stage instead of 4 global loads
# speedup vs baseline: 1.0021x; 1.0021x over previous
.LBB0_403:
	s_cmp_lt_i32 s96, 5
	s_cselect_b64 s[2:3], -1, 0
	s_and_b64 s[4:5], s[2:3], s[0:1]
	s_andn2_b64 vcc, exec, s[4:5]
	s_cbranch_vccnz .LBB0_445
	v_mbcnt_hi_u32_b32 v0, -1, v248
	v_add_u32_e32 v214, s84, v0
	v_readlane_b32 s0, v254, 2
	s_cmpk_gt_i32 s0, 0x3ff
	v_readfirstlane_b32 s0, v214
	v_readlane_b32 s1, v254, 3
	s_cbranch_scc1 .LBB0_445
	v_and_b32_e32 v2, 0x7f, v214
	v_lshlrev_b32_e32 v2, 2, v2
	global_load_dword v3, v2, s[62:63]
	v_add_u32_e32 v2, 0x27e00, v2
	s_waitcnt vmcnt(0)
	ds_write_b32 v2, v3
	s_add_u32 s26, s54, 0x16200000
	s_addc_u32 s27, s55, 0
	s_add_u32 s28, s54, 0x1e200000
	s_addc_u32 s29, s55, 0
	s_add_u32 s30, s54, 0x26200000
	s_addc_u32 s31, s55, 0
	s_add_u32 s34, s54, 0x36200000
	s_addc_u32 s35, s55, 0
	s_ashr_i32 s1, s0, 6
	s_and_b32 s36, s1, 1
	v_add_u32_e32 v1, -1, v0
	v_and_b32_e32 v2, 0x7c, v0
	s_cmp_gt_i32 s1, 3
	v_cmp_lt_i32_e32 vcc, v1, v2
	s_cselect_b64 s[6:7], -1, 0
	s_ashr_i32 s0, s0, 7
	v_cndmask_b32_e32 v1, v1, v0, vcc
	s_lshl_b32 s8, s0, 5
	v_lshlrev_b32_e32 v215, 2, v1
	v_add_u32_e32 v1, -2, v0
	s_ashr_i32 s9, s8, 31
	v_cmp_lt_i32_e32 vcc, v1, v2
	s_lshl_b32 s37, s36, 5
	s_bitcmp1_b32 s1, 0
	v_cndmask_b32_e32 v1, v1, v0, vcc
	v_and_b32_e32 v2, 64, v0
	v_lshlrev_b32_e32 v216, 2, v1
	s_cselect_b64 s[10:11], -1, 0
	v_xor_b32_e32 v1, 32, v0
	v_add_u32_e32 v2, 64, v2
	s_lshl_b32 s1, s0, 8
	v_cmp_lt_i32_e32 vcc, v1, v2
	s_add_i32 s1, s1, 0
	s_lshl_b32 s2, s36, 7
	s_lshl_b32 s0, s0, 6
	v_lshl_or_b32 v217, v0, 2, 12
	v_cndmask_b32_e32 v0, v0, v1, vcc
	s_add_i32 s38, s1, s2
	s_add_i32 s39, s0, 0
	v_readlane_b32 s0, v254, 2
	v_lshlrev_b32_e32 v218, 2, v0
	s_add_i32 s38, s38, 0x27800
	s_add_i32 s39, s39, 0x23400
	v_mov_b32_e32 v1, 0
	s_movk_i32 s40, 0x1000
	s_movk_i32 s41, 0x2000
	s_movk_i32 s42, 0x3000
	s_movk_i32 s43, 0x4000
	s_movk_i32 s46, 0x5000
	s_movk_i32 s47, 0x6000
	s_movk_i32 s48, 0x7000
	s_mov_b32 s49, 0x8000
	s_mov_b32 s50, 0x9000
	s_mov_b32 s51, 0xa000
	s_mov_b32 s56, 0xb000
	s_mov_b32 s57, 0xc000
	s_mov_b32 s58, 0xd000
	s_mov_b32 s59, 0xe000
	s_movk_i32 s60, 0x90
	s_mov_b64 s[12:13], 0x2e200000
	s_mov_b32 s61, 0x2e200000
	s_movk_i32 s64, 0x110
	s_mov_b64 s[14:15], 0x1e240000
	s_mov_b32 s65, 0x1e240000
	s_mov_b64 s[16:17], 0x16240000
	s_mov_b32 s66, 0x16240000
	v_mov_b32_e32 v219, 0x358637bd
	s_mov_b32 s67, s0
	s_mov_b32 s73, s0
	v_readlane_b32 s1, v254, 3
	s_branch .LBB0_407

.LBB0_412:
	s_or_b64 exec, exec, s[2:3]
	s_and_b32 s2, s67, 15
	s_lshl_b32 s75, s2, 20
	s_bitset1_b32 s22, 17
	s_add_u32 s2, s28, s22
	s_addc_u32 s3, s29, s23
	v_lshl_add_u64 v[10:11], s[2:3], 0, v[14:15]
	s_add_u32 s2, s26, s22
	s_addc_u32 s3, s27, s23
	v_lshl_add_u64 v[14:15], s[2:3], 0, v[14:15]
	s_add_u32 s2, s30, s22
	v_lshl_add_u64 v[86:87], v[10:11], 0, v[0:1]
	v_lshl_add_u64 v[14:15], v[14:15], 0, v[0:1]
	s_addc_u32 s3, s31, s23
	global_load_dwordx4 v[10:13], v[86:87], off offset:16
	global_load_dwordx4 v[160:163], v[86:87], off
	global_load_dwordx4 v[168:171], v[14:15], off offset:16
	global_load_dwordx4 v[164:167], v[14:15], off
	v_lshl_add_u64 v[14:15], s[2:3], 0, v[82:83]
	v_add_co_u32_e32 v82, vcc, s41, v14
	v_and_b32_e32 v0, 7, v80
	s_nop 0
	v_addc_co_u32_e32 v83, vcc, 0, v15, vcc
	global_load_dwordx4 v[172:175], v[14:15], off
	global_load_dwordx4 v[176:179], v[82:83], off
	v_ashrrev_i32_e32 v15, 3, v80
	v_mul_lo_u32 v14, v15, s60
	v_and_b32_e32 v80, 0x70, v84
	v_add3_u32 v14, 0, v14, v80
	ds_write_b128 v14, v[2:5] offset:53248
	ds_write_b128 v14, v[6:9] offset:62464
	v_lshlrev_b32_e32 v2, 5, v0
	s_add_i32 s2, 0, 0x23400
	v_add_u32_e32 v14, s2, v2
	s_lshl_b64 s[0:1], s[0:1], 24
	s_lshl_b32 s2, s73, 10
	s_or_b32 s0, s0, s75
	s_and_b32 s2, s2, 0x1c000
	s_or_b32 s2, s0, s2
	s_add_u32 s75, s54, s2
	s_addc_u32 s77, s55, s1
	s_lshl_b32 s2, s73, 4
	s_and_b32 s2, s2, 0x700
	s_or_b32 s0, s0, s2
	s_waitcnt lgkmcnt(0)
	s_add_u32 s0, s54, s0
	v_lshlrev_b32_e32 v0, 6, v0
	v_mov_b32_e32 v3, v1
	s_addc_u32 s1, s55, s1
	s_mov_b32 s74, 0
	v_add_u32_e32 v204, 0x27e00, v0
	v_lshl_add_u64 v[206:207], s[0:1], 0, v[2:3]
	s_mov_b64 s[22:23], 0
	s_waitcnt lgkmcnt(0)
	s_barrier
	s_branch .LBB0_415

.LBB0_414:
	s_waitcnt lgkmcnt(0)
	s_waitcnt lgkmcnt(0)
	s_barrier
	ds_read_b128 v[10:13], v204
	ds_read_b128 v[16:19], v204 offset:16
	ds_read_b128 v[20:23], v204 offset:32
	ds_read_b128 v[24:27], v204 offset:48
	v_lshl_add_u32 v0, v212, 2, 0
	v_mad_u64_u32 v[28:29], s[0:1], v212, s64, v[14:15]
	s_waitcnt vmcnt(1)
	v_lshlrev_b32_e32 v30, 16, v6
	v_and_b32_e32 v31, 0xffff0000, v6
	v_lshlrev_b32_e32 v32, 16, v7
	v_and_b32_e32 v33, 0xffff0000, v7
	v_lshlrev_b32_e32 v34, 16, v8
	v_and_b32_e32 v35, 0xffff0000, v8
	v_lshlrev_b32_e32 v36, 16, v9
	v_and_b32_e32 v37, 0xffff0000, v9
	s_waitcnt vmcnt(0)
	v_lshlrev_b32_e32 v38, 16, v2
	v_and_b32_e32 v39, 0xffff0000, v2
	v_lshlrev_b32_e32 v40, 16, v3
	v_and_b32_e32 v41, 0xffff0000, v3
	v_lshlrev_b32_e32 v42, 16, v4
	v_and_b32_e32 v43, 0xffff0000, v4
	v_lshlrev_b32_e32 v44, 16, v5
	v_and_b32_e32 v45, 0xffff0000, v5
	ds_read_b128 v[2:5], v28
	v_add_u32_e32 v0, 0x27800, v0
	ds_read_b128 v[6:9], v28 offset:16
	ds_read2st64_b32 v[28:29], v0 offset1:1
	ds_read2st64_b32 v[46:47], v0 offset0:2 offset1:3
	s_add_i32 s74, s74, 1
	s_add_u32 s22, s22, 0x20000
	s_waitcnt lgkmcnt(3)
	v_lshlrev_b32_e32 v48, 16, v2
	s_waitcnt lgkmcnt(1)
	v_mov_b32_e32 v56, v28
	s_waitcnt lgkmcnt(0)
	v_mov_b32_e32 v57, v46
	v_mov_b32_e32 v46, v29
	v_pk_add_f32 v[28:29], v[56:57], v[46:47]
	v_and_b32_e32 v49, 0xffff0000, v2
	v_add_f32_e32 v0, v28, v29
	v_fmamk_f32 v0, v0, 0x3c000000, v219
	v_rsq_f32_e32 v0, v0
	v_lshlrev_b32_e32 v2, 16, v3
	v_and_b32_e32 v3, 0xffff0000, v3
	v_lshlrev_b32_e32 v50, 16, v4
	v_and_b32_e32 v51, 0xffff0000, v4
	v_lshlrev_b32_e32 v4, 16, v5
	v_and_b32_e32 v5, 0xffff0000, v5
	v_lshlrev_b32_e32 v52, 16, v6
	v_and_b32_e32 v53, 0xffff0000, v6
	v_lshlrev_b32_e32 v6, 16, v7
	v_and_b32_e32 v7, 0xffff0000, v7
	v_pk_mul_f32 v[2:3], v[0:1], v[2:3] op_sel_hi:[0,1]
	v_pk_mul_f32 v[28:29], v[0:1], v[48:49] op_sel_hi:[0,1]
	v_pk_mul_f32 v[4:5], v[0:1], v[4:5] op_sel_hi:[0,1]
	v_pk_mul_f32 v[46:47], v[0:1], v[50:51] op_sel_hi:[0,1]
	v_pk_mul_f32 v[6:7], v[0:1], v[6:7] op_sel_hi:[0,1]
	v_pk_mul_f32 v[48:49], v[0:1], v[52:53] op_sel_hi:[0,1]
	v_lshlrev_b32_e32 v54, 16, v8
	v_and_b32_e32 v55, 0xffff0000, v8
	v_lshlrev_b32_e32 v8, 16, v9
	v_and_b32_e32 v9, 0xffff0000, v9
	v_pk_mul_f32 v[8:9], v[0:1], v[8:9] op_sel_hi:[0,1]
	v_pk_mul_f32 v[50:51], v[0:1], v[54:55] op_sel_hi:[0,1]
	s_addc_u32 s23, s23, 0
	v_mov_b64_e32 v[64:65], v[80:81]
	v_mov_b64_e32 v[160:161], v[180:181]
	v_mov_b64_e32 v[176:177], v[196:197]
	v_mov_b64_e32 v[172:173], v[200:201]
	v_mov_b64_e32 v[168:169], v[184:185]
	v_mov_b64_e32 v[164:165], v[192:193]
	s_cmp_eq_u32 s22, 0x100000
	v_mov_b64_e32 v[66:67], v[82:83]
	v_mov_b64_e32 v[68:69], v[84:85]
	v_mov_b64_e32 v[70:71], v[86:87]
	v_mov_b64_e32 v[72:73], v[88:89]
	v_mov_b64_e32 v[74:75], v[90:91]
	v_mov_b64_e32 v[76:77], v[92:93]
	v_mov_b64_e32 v[78:79], v[94:95]
	v_mov_b64_e32 v[162:163], v[182:183]
	v_mov_b64_e32 v[178:179], v[198:199]
	v_mov_b64_e32 v[174:175], v[202:203]
	v_mov_b64_e32 v[170:171], v[186:187]
	v_mov_b64_e32 v[166:167], v[194:195]
	s_waitcnt vmcnt(3)
	v_pk_mul_f32 v[10:11], v[10:11], v[28:29]
	v_pk_mul_f32 v[2:3], v[12:13], v[2:3]
	s_waitcnt vmcnt(2)
	v_pk_mul_f32 v[12:13], v[16:17], v[46:47]
	v_pk_mul_f32 v[4:5], v[18:19], v[4:5]
	s_waitcnt vmcnt(1)
	v_pk_mul_f32 v[16:17], v[20:21], v[48:49]
	v_pk_mul_f32 v[6:7], v[22:23], v[6:7]
	v_pk_mul_f32 v[20:21], v[2:3], v[32:33]
	v_pk_mul_f32 v[2:3], v[10:11], v[30:31]
	v_pk_mul_f32 v[10:11], v[4:5], v[36:37]
	v_pk_mul_f32 v[4:5], v[12:13], v[34:35]
	v_pk_mul_f32 v[6:7], v[6:7], v[40:41]
	v_cvt_pk_bf16_f32 v2, v2, v3
	v_cvt_pk_bf16_f32 v3, v20, v21
	v_pk_mul_f32 v[12:13], v[16:17], v[38:39]
	v_cvt_pk_bf16_f32 v4, v4, v5
	v_cvt_pk_bf16_f32 v5, v10, v11
	global_store_dwordx4 v[210:211], v[2:5], off
	s_waitcnt vmcnt(1)
	v_pk_mul_f32 v[18:19], v[24:25], v[50:51]
	v_pk_mul_f32 v[8:9], v[26:27], v[8:9]
	v_cvt_pk_bf16_f32 v2, v12, v13
	v_cvt_pk_bf16_f32 v3, v6, v7
	v_add_co_u32_e32 v6, vcc, s61, v208
	v_pk_mul_f32 v[8:9], v[8:9], v[44:45]
	s_nop 0
	v_addc_co_u32_e32 v7, vcc, 0, v209, vcc
	v_pk_mul_f32 v[16:17], v[18:19], v[42:43]
	v_mov_b64_e32 v[48:49], v[128:129]
	v_cvt_pk_bf16_f32 v4, v16, v17
	v_cvt_pk_bf16_f32 v5, v8, v9
	global_store_dwordx4 v[6:7], v[2:5], off offset:16
	s_waitcnt lgkmcnt(0)
	v_mov_b64_e32 v[32:33], v[112:113]
	v_mov_b64_e32 v[16:17], v[96:97]
	v_mov_b64_e32 v[10:11], v[188:189]
	v_mov_b64_e32 v[50:51], v[130:131]
	v_mov_b64_e32 v[52:53], v[132:133]
	v_mov_b64_e32 v[54:55], v[134:135]
	v_mov_b64_e32 v[56:57], v[136:137]
	v_mov_b64_e32 v[58:59], v[138:139]
	v_mov_b64_e32 v[60:61], v[140:141]
	v_mov_b64_e32 v[62:63], v[142:143]
	v_mov_b64_e32 v[34:35], v[114:115]
	v_mov_b64_e32 v[36:37], v[116:117]
	v_mov_b64_e32 v[38:39], v[118:119]
	v_mov_b64_e32 v[40:41], v[120:121]
	v_mov_b64_e32 v[42:43], v[122:123]
	v_mov_b64_e32 v[44:45], v[124:125]
	v_mov_b64_e32 v[46:47], v[126:127]
	v_mov_b64_e32 v[18:19], v[98:99]
	v_mov_b64_e32 v[20:21], v[100:101]
	v_mov_b64_e32 v[22:23], v[102:103]
	v_mov_b64_e32 v[24:25], v[104:105]
	v_mov_b64_e32 v[26:27], v[106:107]
	v_mov_b64_e32 v[28:29], v[108:109]
	v_mov_b64_e32 v[30:31], v[110:111]
	v_mov_b64_e32 v[12:13], v[190:191]
	s_barrier
	s_cbranch_scc1 .LBB0_406
